# C2 copy of the q_lat weight-fold loop: 20 loads per 4-d group issued together (was ~6 serialized load/wait rounds per iteration), plain f32 fmac instead of gather-movs + pk_fma
# baseline (speedup 1.0000x reference)
.LBB0_2126:
	s_add_u32 s38, s4, s6
	s_addc_u32 s39, s33, s7
	s_waitcnt vmcnt(4)
	global_load_dwordx2 v[138:139], v[106:107], off offset:-1540
	global_load_dwordx2 v[178:179], v[106:107], off offset:-1028
	global_load_dwordx2 v[194:195], v[106:107], off offset:-516
	global_load_dwordx2 v[196:197], v[106:107], off offset:-4
	global_load_dwordx4 v[2:5], v1, s[38:39]
	v_mov_b32_e32 v0, 0x2000
	global_load_dwordx4 v[6:9], v0, s[38:39] offset:2848
	v_mov_b32_e32 v0, 0x5000
	global_load_dwordx4 v[10:13], v0, s[38:39] offset:1600
	s_waitcnt lgkmcnt(0)
	global_load_dwordx4 v[14:17], v229, s[38:39] offset:352
	v_mov_b32_e32 v0, 0xa000
	global_load_dwordx4 v[130:133], v0, s[38:39] offset:3200
	v_mov_b32_e32 v0, 0xd000
	global_load_dwordx4 v[134:137], v0, s[38:39] offset:1952
	v_mov_b32_e32 v0, 0x10000
	global_load_dwordx4 v[150:153], v0, s[38:39] offset:704
	v_mov_b32_e32 v0, 0x12000
	global_load_dwordx4 v[154:157], v0, s[38:39] offset:3552
	v_mov_b32_e32 v0, 0x15000
	global_load_dwordx4 v[158:161], v0, s[38:39] offset:2304
	v_mov_b32_e32 v0, 0x18000
	global_load_dwordx4 v[162:165], v0, s[38:39] offset:1056
	v_mov_b32_e32 v0, 0x1a000
	global_load_dwordx4 v[166:169], v0, s[38:39] offset:3904
	v_mov_b32_e32 v0, 0x1d000
	global_load_dwordx4 v[170:173], v0, s[38:39] offset:2656
	v_mov_b32_e32 v0, 0x20000
	global_load_dwordx4 v[174:177], v0, s[38:39] offset:1408
	v_mov_b32_e32 v0, 0x23000
	global_load_dwordx4 v[182:185], v0, s[38:39] offset:160
	v_mov_b32_e32 v0, 0x25000
	global_load_dwordx4 v[186:189], v0, s[38:39] offset:3008
	v_mov_b32_e32 v0, 0x28000
	global_load_dwordx4 v[190:193], v0, s[38:39] offset:1760
	s_add_u32 s6, s6, 16
	s_addc_u32 s7, s7, 0
	s_cmpk_lg_i32 s6, 0x100
	s_mov_b64 s[38:39], 0x800
	v_lshl_add_u64 v[106:107], v[106:107], 0, s[38:39]
	s_waitcnt vmcnt(0)
	v_fmac_f32_e32 v22, v138, v2
	v_fmac_f32_e32 v30, v139, v2
	v_fmac_f32_e32 v18, v138, v6
	v_fmac_f32_e32 v26, v139, v6
	v_fmac_f32_e32 v23, v138, v10
	v_fmac_f32_e32 v31, v139, v10
	v_fmac_f32_e32 v19, v138, v14
	v_fmac_f32_e32 v27, v139, v14
	v_fmac_f32_e32 v38, v138, v130
	v_fmac_f32_e32 v46, v139, v130
	v_fmac_f32_e32 v34, v138, v134
	v_fmac_f32_e32 v42, v139, v134
	v_fmac_f32_e32 v39, v138, v150
	v_fmac_f32_e32 v47, v139, v150
	v_fmac_f32_e32 v35, v138, v154
	v_fmac_f32_e32 v43, v139, v154
	v_fmac_f32_e32 v54, v138, v158
	v_fmac_f32_e32 v62, v139, v158
	v_fmac_f32_e32 v50, v138, v162
	v_fmac_f32_e32 v58, v139, v162
	v_fmac_f32_e32 v55, v138, v166
	v_fmac_f32_e32 v63, v139, v166
	v_fmac_f32_e32 v51, v138, v170
	v_fmac_f32_e32 v59, v139, v170
	v_fmac_f32_e32 v108, v138, v174
	v_fmac_f32_e32 v114, v139, v174
	v_fmac_f32_e32 v110, v138, v182
	v_fmac_f32_e32 v112, v139, v182
	v_fmac_f32_e32 v109, v138, v186
	v_fmac_f32_e32 v115, v139, v186
	v_fmac_f32_e32 v111, v138, v190
	v_fmac_f32_e32 v113, v139, v190
	v_fmac_f32_e32 v22, v178, v3
	v_fmac_f32_e32 v30, v179, v3
	v_fmac_f32_e32 v18, v178, v7
	v_fmac_f32_e32 v26, v179, v7
	v_fmac_f32_e32 v23, v178, v11
	v_fmac_f32_e32 v31, v179, v11
	v_fmac_f32_e32 v19, v178, v15
	v_fmac_f32_e32 v27, v179, v15
	v_fmac_f32_e32 v38, v178, v131
	v_fmac_f32_e32 v46, v179, v131
	v_fmac_f32_e32 v34, v178, v135
	v_fmac_f32_e32 v42, v179, v135
	v_fmac_f32_e32 v39, v178, v151
	v_fmac_f32_e32 v47, v179, v151
	v_fmac_f32_e32 v35, v178, v155
	v_fmac_f32_e32 v43, v179, v155
	v_fmac_f32_e32 v54, v178, v159
	v_fmac_f32_e32 v62, v179, v159
	v_fmac_f32_e32 v50, v178, v163
	v_fmac_f32_e32 v58, v179, v163
	v_fmac_f32_e32 v55, v178, v167
	v_fmac_f32_e32 v63, v179, v167
	v_fmac_f32_e32 v51, v178, v171
	v_fmac_f32_e32 v59, v179, v171
	v_fmac_f32_e32 v108, v178, v175
	v_fmac_f32_e32 v114, v179, v175
	v_fmac_f32_e32 v110, v178, v183
	v_fmac_f32_e32 v112, v179, v183
	v_fmac_f32_e32 v109, v178, v187
	v_fmac_f32_e32 v115, v179, v187
	v_fmac_f32_e32 v111, v178, v191
	v_fmac_f32_e32 v113, v179, v191
	v_fmac_f32_e32 v22, v194, v4
	v_fmac_f32_e32 v30, v195, v4
	v_fmac_f32_e32 v18, v194, v8
	v_fmac_f32_e32 v26, v195, v8
	v_fmac_f32_e32 v23, v194, v12
	v_fmac_f32_e32 v31, v195, v12
	v_fmac_f32_e32 v19, v194, v16
	v_fmac_f32_e32 v27, v195, v16
	v_fmac_f32_e32 v38, v194, v132
	v_fmac_f32_e32 v46, v195, v132
	v_fmac_f32_e32 v34, v194, v136
	v_fmac_f32_e32 v42, v195, v136
	v_fmac_f32_e32 v39, v194, v152
	v_fmac_f32_e32 v47, v195, v152
	v_fmac_f32_e32 v35, v194, v156
	v_fmac_f32_e32 v43, v195, v156
	v_fmac_f32_e32 v54, v194, v160
	v_fmac_f32_e32 v62, v195, v160
	v_fmac_f32_e32 v50, v194, v164
	v_fmac_f32_e32 v58, v195, v164
	v_fmac_f32_e32 v55, v194, v168
	v_fmac_f32_e32 v63, v195, v168
	v_fmac_f32_e32 v51, v194, v172
	v_fmac_f32_e32 v59, v195, v172
	v_fmac_f32_e32 v108, v194, v176
	v_fmac_f32_e32 v114, v195, v176
	v_fmac_f32_e32 v110, v194, v184
	v_fmac_f32_e32 v112, v195, v184
	v_fmac_f32_e32 v109, v194, v188
	v_fmac_f32_e32 v115, v195, v188
	v_fmac_f32_e32 v111, v194, v192
	v_fmac_f32_e32 v113, v195, v192
	v_fmac_f32_e32 v22, v196, v5
	v_fmac_f32_e32 v30, v197, v5
	v_fmac_f32_e32 v18, v196, v9
	v_fmac_f32_e32 v26, v197, v9
	v_fmac_f32_e32 v23, v196, v13
	v_fmac_f32_e32 v31, v197, v13
	v_fmac_f32_e32 v19, v196, v17
	v_fmac_f32_e32 v27, v197, v17
	v_fmac_f32_e32 v38, v196, v133
	v_fmac_f32_e32 v46, v197, v133
	v_fmac_f32_e32 v34, v196, v137
	v_fmac_f32_e32 v42, v197, v137
	v_fmac_f32_e32 v39, v196, v153
	v_fmac_f32_e32 v47, v197, v153
	v_fmac_f32_e32 v35, v196, v157
	v_fmac_f32_e32 v43, v197, v157
	v_fmac_f32_e32 v54, v196, v161
	v_fmac_f32_e32 v62, v197, v161
	v_fmac_f32_e32 v50, v196, v165
	v_fmac_f32_e32 v58, v197, v165
	v_fmac_f32_e32 v55, v196, v169
	v_fmac_f32_e32 v63, v197, v169
	v_fmac_f32_e32 v51, v196, v173
	v_fmac_f32_e32 v59, v197, v173
	v_fmac_f32_e32 v108, v196, v177
	v_fmac_f32_e32 v114, v197, v177
	v_fmac_f32_e32 v110, v196, v185
	v_fmac_f32_e32 v112, v197, v185
	v_fmac_f32_e32 v109, v196, v189
	v_fmac_f32_e32 v115, v197, v189
	v_fmac_f32_e32 v111, v196, v193
	v_fmac_f32_e32 v113, v197, v193
	s_cbranch_scc1 .LBB0_2126
	s_lshl_b32 s4, s85, 4
	s_and_b32 s4, s4, 0x3f0
	s_lshl_b32 s6, s4, 2
	v_mov_b32_e32 v0, s6
	global_load_dwordx4 v[10:13], v0, s[10:11] offset:48
	global_load_dwordx4 v[14:17], v0, s[10:11] offset:32
	global_load_dwordx4 v[2:5], v0, s[10:11] offset:16
	global_load_dwordx4 v[6:9], v0, s[10:11]
	s_mov_b32 s6, 0xffff0000
	s_lshl_b32 s96, s4, 1
	s_waitcnt vmcnt(0)
	v_mov_b32_e32 v21, v8
	v_mov_b32_e32 v8, v7
	v_mov_b32_e32 v20, v6
	v_pk_mul_f32 v[6:7], v[26:27], v[8:9]
	v_pk_mul_f32 v[8:9], v[18:19], v[8:9]
	v_mov_b32_e32 v19, v4
	v_mov_b32_e32 v4, v3
	v_mov_b32_e32 v18, v2
	v_pk_mul_f32 v[26:27], v[42:43], v[4:5]
	v_pk_mul_f32 v[4:5], v[34:35], v[4:5]
	v_pk_mul_f32 v[24:25], v[30:31], v[20:21]
	v_pk_mul_f32 v[20:21], v[22:23], v[20:21]
	v_pk_mul_f32 v[22:23], v[46:47], v[18:19]
	v_pk_mul_f32 v[2:3], v[38:39], v[18:19]
	v_bfe_u32 v18, v4, 16, 1
	v_bfe_u32 v28, v8, 16, 1
	v_bfe_u32 v0, v5, 16, 1
	v_add3_u32 v8, v8, v28, s55
	v_add3_u32 v4, v4, v18, s55
	v_bfe_u32 v18, v21, 16, 1
	v_bfe_u32 v28, v3, 16, 1
	v_bfe_u32 v19, v9, 16, 1
	v_add3_u32 v0, v5, v0, s55
	v_bfe_u32 v5, v20, 16, 1
	v_add3_u32 v3, v3, v28, s55
	v_add3_u32 v18, v21, v18, s55
	v_add3_u32 v9, v9, v19, s55
	v_bfe_u32 v19, v2, 16, 1
	v_add3_u32 v5, v20, v5, s55
	v_lshrrev_b32_e32 v18, 16, v18
	v_lshrrev_b32_e32 v3, 16, v3
	v_add3_u32 v2, v2, v19, s55
	v_lshrrev_b32_e32 v19, 16, v5
	v_and_or_b32 v5, v0, s6, v3
	v_and_or_b32 v3, v9, s6, v18
	v_bfe_u32 v9, v7, 16, 1
	v_add3_u32 v7, v7, v9, s55
	v_bfe_u32 v9, v24, 16, 1
	v_lshrrev_b32_e32 v2, 16, v2
	v_bfe_u32 v18, v6, 16, 1
	v_add3_u32 v9, v24, v9, s55
	v_and_or_b32 v4, v4, s6, v2
	v_and_or_b32 v2, v8, s6, v19
	v_add3_u32 v6, v6, v18, s55
	v_bfe_u32 v18, v25, 16, 1
	v_bfe_u32 v19, v22, 16, 1
	v_bfe_u32 v20, v23, 16, 1
	v_lshrrev_b32_e32 v21, 16, v9
	v_bfe_u32 v0, v27, 16, 1
	v_bfe_u32 v8, v26, 16, 1
	v_add3_u32 v20, v23, v20, s55
	v_add3_u32 v19, v22, v19, s55
	v_add3_u32 v18, v25, v18, s55
	v_and_or_b32 v6, v6, s6, v21
	v_mov_b32_e32 v21, v16
	v_mov_b32_e32 v16, v15
	v_mov_b32_e32 v25, v12
	v_mov_b32_e32 v12, v11
	v_add3_u32 v8, v26, v8, s55
	v_add3_u32 v0, v27, v0, s55
	v_lshrrev_b32_e32 v18, 16, v18
	v_lshrrev_b32_e32 v19, 16, v19
	v_lshrrev_b32_e32 v9, 16, v20
	v_mov_b32_e32 v20, v14
	v_pk_mul_f32 v[22:23], v[50:51], v[16:17]
	v_mov_b32_e32 v24, v10
	v_pk_mul_f32 v[26:27], v[112:113], v[12:13]
	v_pk_mul_f32 v[12:13], v[110:111], v[12:13]
	v_and_or_b32 v9, v0, s6, v9
	v_and_or_b32 v8, v8, s6, v19
	v_and_or_b32 v7, v7, s6, v18
	v_pk_mul_f32 v[18:19], v[62:63], v[20:21]
	v_pk_mul_f32 v[14:15], v[58:59], v[16:17]
	v_pk_mul_f32 v[20:21], v[54:55], v[20:21]
	v_pk_mul_f32 v[16:17], v[114:115], v[24:25]
	v_pk_mul_f32 v[10:11], v[108:109], v[24:25]
	v_bfe_u32 v0, v13, 16, 1
	v_bfe_u32 v24, v12, 16, 1
	v_bfe_u32 v25, v23, 16, 1
	v_bfe_u32 v28, v22, 16, 1
	v_add3_u32 v22, v22, v28, s55
	v_add3_u32 v23, v23, v25, s55
	v_add3_u32 v12, v12, v24, s55
	v_add3_u32 v0, v13, v0, s55
	v_bfe_u32 v13, v20, 16, 1
	v_bfe_u32 v24, v21, 16, 1
	v_bfe_u32 v25, v10, 16, 1
	v_bfe_u32 v28, v11, 16, 1
	v_add3_u32 v11, v11, v28, s55
	v_add3_u32 v10, v10, v25, s55
	v_add3_u32 v21, v21, v24, s55
	v_add3_u32 v13, v20, v13, s55
	v_lshrrev_b32_e32 v20, 16, v13
	v_lshrrev_b32_e32 v21, 16, v21
	v_lshrrev_b32_e32 v10, 16, v10
	v_lshrrev_b32_e32 v11, 16, v11
	v_and_or_b32 v13, v0, s6, v11
	v_and_or_b32 v12, v12, s6, v10
	v_and_or_b32 v11, v23, s6, v21
	v_and_or_b32 v10, v22, s6, v20
	v_bfe_u32 v21, v15, 16, 1
	v_bfe_u32 v22, v14, 16, 1
	v_add3_u32 v14, v14, v22, s55
	v_add3_u32 v15, v15, v21, s55
	v_bfe_u32 v21, v18, 16, 1
	v_bfe_u32 v22, v19, 16, 1
	v_bfe_u32 v23, v16, 16, 1
	v_bfe_u32 v24, v17, 16, 1
	v_bfe_u32 v0, v27, 16, 1
	v_bfe_u32 v20, v26, 16, 1
	v_add3_u32 v17, v17, v24, s55
	v_add3_u32 v16, v16, v23, s55
	v_add3_u32 v19, v19, v22, s55
	v_add3_u32 v18, v18, v21, s55
	v_add3_u32 v20, v26, v20, s55
	v_add3_u32 v0, v27, v0, s55
	v_lshrrev_b32_e32 v18, 16, v18
	v_lshrrev_b32_e32 v19, 16, v19
	v_lshrrev_b32_e32 v16, 16, v16
	v_lshrrev_b32_e32 v17, 16, v17
	v_and_or_b32 v17, v0, s6, v17
	v_and_or_b32 v16, v20, s6, v16
	v_and_or_b32 v15, v15, s6, v19
	v_and_or_b32 v14, v14, s6, v18
	s_and_b32 s6, s85, 0x7fffffc0
	v_or_b32_e32 v0, s6, v148
	v_lshlrev_b32_e32 v18, 1, v0
	v_ashrrev_i32_e32 v19, 31, v18
	v_lshlrev_b64 v[20:21], 11, v[18:19]
	v_or_b32_e32 v18, 1, v18
	v_ashrrev_i32_e32 v19, 31, v18
	v_lshl_add_u64 v[20:21], s[12:13], 0, v[20:21]
	v_lshlrev_b64 v[18:19], 11, v[18:19]
	v_lshl_add_u64 v[20:21], v[20:21], 0, s[96:97]
	v_lshl_add_u64 v[18:19], s[12:13], 0, v[18:19]
	v_lshl_add_u64 v[18:19], v[18:19], 0, s[96:97]
	global_store_dwordx4 v[20:21], v[2:5], off
	global_store_dwordx4 v[20:21], v[10:13], off offset:16
	global_store_dwordx4 v[18:19], v[6:9], off
	global_store_dwordx4 v[18:19], v[14:17], off offset:16
	s_branch .LBB0_1810
